# MLA step: row-max / rescale decision moved into the shadow of P.V MFMAs 1-3 (they do not depend on it); the 24 exp2 dealt 6 per gap behind P.V MFMAs 4-7
# speedup vs baseline: 1.0009x; 1.0009x over previous
.LBB0_1152:
	s_waitcnt lgkmcnt(0)
	v_mfma_f32_32x32x16_bf16 v[4:19], v[140:143], v[172:175], v[4:19]
	v_max_f32_e32 v64, v101, v100
	v_max3_f32 v65, v102, v103, v85
	v_max3_f32 v64, v64, v84, v86
	v_max3_f32 v64, v64, v87, v104
	v_max3_f32 v65, v65, v106, v107
	v_max3_f32 v64, v64, v105, v88
	v_max3_f32 v65, v65, v90, v91
	v_max3_f32 v64, v64, v89, v108
	v_mfma_f32_32x32x16_bf16 v[20:35], v[140:143], v[68:71], v[20:35]
	s_and_b32 s12, s27, 3
	s_mulk_i32 s12, 0x3000
	v_add_u32_e32 v140, s12, v188
	v_lshl_add_u32 v141, s18, 13, v186
	ds_read_b128 v[202:205], v140
	ds_read_b128 v[190:193], v140 offset:512
	ds_read_b128 v[194:197], v140 offset:2048
	ds_read_b128 v[198:201], v140 offset:2560
	v_max3_f32 v65, v65, v110, v111
	v_max3_f32 v64, v64, v109, v92
	v_max3_f32 v65, v65, v94, v95
	v_max3_f32 v64, v64, v93, v112
	v_mfma_f32_32x32x16_bf16 v[4:19], v[144:147], v[72:75], v[4:19]
	v_max3_f32 v65, v65, v114, v115
	v_max3_f32 v64, v64, v113, v96
	v_max3_f32 v65, v65, v98, v99
	v_max3_f32 v64, v64, v97, v65
	v_mov_b32_e32 v65, v64
	s_nop 1
	v_permlane32_swap_b32_e32 v64, v65
	v_max_f32_e32 v64, v64, v65
	v_cmp_lt_f32_e32 vcc, s81, v64
	s_cmp_lg_u64 vcc, 0
	v_add_f32_e32 v189, v189, v156
	s_cselect_b64 s[10:11], -1, 0
	s_cbranch_vccnz .LBB0_1168
.LBB0_1153:
	v_mfma_f32_32x32x16_bf16 v[20:35], v[144:147], v[76:79], v[20:35]
	v_exp_f32_e32 v100, v100
	v_exp_f32_e32 v101, v101
	v_exp_f32_e32 v102, v102
	v_exp_f32_e32 v103, v103
	v_exp_f32_e32 v104, v104
	v_exp_f32_e32 v105, v105
	v_mfma_f32_32x32x16_bf16 v[4:19], v[148:151], v[80:83], v[4:19]
	v_exp_f32_e32 v106, v106
	v_exp_f32_e32 v107, v107
	v_exp_f32_e32 v108, v108
	v_exp_f32_e32 v109, v109
	v_exp_f32_e32 v110, v110
	v_exp_f32_e32 v111, v111
	v_mfma_f32_32x32x16_bf16 v[20:35], v[148:151], v[52:55], v[20:35]
	v_exp_f32_e32 v112, v112
	v_exp_f32_e32 v113, v113
	v_exp_f32_e32 v114, v114
	v_exp_f32_e32 v115, v115
	v_exp_f32_e32 v84, v84
	v_exp_f32_e32 v85, v85
	v_mfma_f32_32x32x16_bf16 v[4:19], v[152:155], v[56:59], v[4:19]
	v_exp_f32_e32 v86, v86
	v_exp_f32_e32 v87, v87
	v_exp_f32_e32 v88, v88
	v_exp_f32_e32 v89, v89
	v_exp_f32_e32 v90, v90
	v_exp_f32_e32 v91, v91
	v_mfma_f32_32x32x16_bf16 v[20:35], v[152:155], v[60:63], v[20:35]
	s_and_b64 vcc, exec, s[10:11]
	s_cbranch_vccnz .Lmla_resc1

.LBB0_1162:
	s_waitcnt lgkmcnt(0)
	v_mfma_f32_32x32x16_bf16 v[4:19], v[156:159], v[172:175], v[4:19]
	v_max_f32_e32 v96, v69, v68
	v_max3_f32 v97, v70, v71, v53
	v_max3_f32 v96, v96, v52, v54
	v_max3_f32 v96, v96, v55, v72
	v_max3_f32 v97, v97, v74, v75
	v_max3_f32 v96, v96, v73, v56
	v_max3_f32 v97, v97, v58, v59
	v_max3_f32 v96, v96, v57, v76
	v_mfma_f32_32x32x16_bf16 v[20:35], v[156:159], v[100:103], v[20:35]
	s_add_i32 s12, s16, -1
	s_and_b32 s12, s12, 3
	s_mulk_i32 s12, 0x3000
	v_add_u32_e32 v156, s12, v188
	s_add_i32 s12, s14, 0x4000
	s_and_b32 s12, s12, 0x6000
	v_add_u32_e32 v157, s12, v186
	ds_read_b128 v[202:205], v156
	ds_read_b128 v[190:193], v156 offset:512
	ds_read_b128 v[194:197], v156 offset:2048
	ds_read_b128 v[198:201], v156 offset:2560
	v_max3_f32 v97, v97, v78, v79
	v_max3_f32 v96, v96, v77, v60
	v_max3_f32 v97, v97, v62, v63
	v_max3_f32 v96, v96, v61, v80
	v_mfma_f32_32x32x16_bf16 v[4:19], v[160:163], v[104:107], v[4:19]
	v_max3_f32 v97, v97, v82, v83
	v_max3_f32 v96, v96, v81, v64
	v_max3_f32 v97, v97, v66, v67
	v_max3_f32 v96, v96, v65, v97
	v_mov_b32_e32 v97, v96
	s_nop 1
	v_permlane32_swap_b32_e32 v96, v97
	v_max_f32_e32 v96, v96, v97
	v_cmp_lt_f32_e32 vcc, s81, v96
	s_cmp_lg_u64 vcc, 0
	v_add_f32_e32 v189, v189, v140
	s_cselect_b64 s[10:11], -1, 0
	s_cbranch_vccnz .LBB0_1172
.LBB0_1163:
	v_mfma_f32_32x32x16_bf16 v[20:35], v[160:163], v[108:111], v[20:35]
	v_exp_f32_e32 v68, v68
	v_exp_f32_e32 v69, v69
	v_exp_f32_e32 v70, v70
	v_exp_f32_e32 v71, v71
	v_exp_f32_e32 v72, v72
	v_exp_f32_e32 v73, v73
	v_mfma_f32_32x32x16_bf16 v[4:19], v[164:167], v[112:115], v[4:19]
	v_exp_f32_e32 v74, v74
	v_exp_f32_e32 v75, v75
	v_exp_f32_e32 v76, v76
	v_exp_f32_e32 v77, v77
	v_exp_f32_e32 v78, v78
	v_exp_f32_e32 v79, v79
	v_mfma_f32_32x32x16_bf16 v[20:35], v[164:167], v[84:87], v[20:35]
	v_exp_f32_e32 v80, v80
	v_exp_f32_e32 v81, v81
	v_exp_f32_e32 v82, v82
	v_exp_f32_e32 v83, v83
	v_exp_f32_e32 v52, v52
	v_exp_f32_e32 v53, v53
	v_mfma_f32_32x32x16_bf16 v[4:19], v[168:171], v[88:91], v[4:19]
	v_exp_f32_e32 v54, v54
	v_exp_f32_e32 v55, v55
	v_exp_f32_e32 v56, v56
	v_exp_f32_e32 v57, v57
	v_exp_f32_e32 v58, v58
	v_exp_f32_e32 v59, v59
	v_mfma_f32_32x32x16_bf16 v[20:35], v[168:171], v[92:95], v[20:35]
	s_and_b64 vcc, exec, s[10:11]
	s_cbranch_vccnz .Lmla_resc2
